# gather rows staged through LDS by LDS-DMA (global_load_lds_dwordx4) in the wide-load layout; cvt with 16B sc1 stores
# speedup vs baseline: 1.0003x; 1.0003x over previous
	.amdhsa_kernel _Z10cvt_kernelPKDv4_fPDv4_DF16_
		.amdhsa_group_segment_fixed_size 0
		.amdhsa_private_segment_fixed_size 0
		.amdhsa_kernarg_size 16
		.amdhsa_user_sgpr_count 2
		.amdhsa_user_sgpr_dispatch_ptr 0
		.amdhsa_user_sgpr_queue_ptr 0
		.amdhsa_user_sgpr_kernarg_segment_ptr 1
		.amdhsa_user_sgpr_dispatch_id 0
		.amdhsa_user_sgpr_kernarg_preload_length 0
		.amdhsa_user_sgpr_kernarg_preload_offset 0
		.amdhsa_user_sgpr_private_segment_size 0
		.amdhsa_uses_dynamic_stack 0
		.amdhsa_enable_private_segment 0
		.amdhsa_system_sgpr_workgroup_id_x 1
		.amdhsa_system_sgpr_workgroup_id_y 0
		.amdhsa_system_sgpr_workgroup_id_z 0
		.amdhsa_system_sgpr_workgroup_info 0
		.amdhsa_system_vgpr_workitem_id 0
		.amdhsa_next_free_vgpr 38
		.amdhsa_next_free_sgpr 18
		.amdhsa_accum_offset 40
		.amdhsa_reserve_vcc 1
		.amdhsa_float_round_mode_32 0
		.amdhsa_float_round_mode_16_64 0
		.amdhsa_float_denorm_mode_32 3
		.amdhsa_float_denorm_mode_16_64 3
		.amdhsa_dx10_clamp 1
		.amdhsa_ieee_mode 1
		.amdhsa_fp16_overflow 0
		.amdhsa_tg_split 0
		.amdhsa_exception_fp_ieee_invalid_op 0
		.amdhsa_exception_fp_denorm_src 0
		.amdhsa_exception_fp_ieee_div_zero 0
		.amdhsa_exception_fp_ieee_overflow 0
		.amdhsa_exception_fp_ieee_underflow 0
		.amdhsa_exception_fp_ieee_inexact 0
		.amdhsa_exception_int_div_zero 0
	.end_amdhsa_kernel

_Z13gather_kernelPKDv2_DF16_PKiPf:
	s_load_dwordx4 s[8:11], s[0:1], 0x0
	s_load_dwordx2 s[4:5], s[0:1], 0x10
	s_lshl_b32 s0, s2, 11
	s_and_b32 s0, s0, 0x3800
	s_lshr_b32 s1, s2, 3
	s_add_i32 s0, s0, s1
	v_lshrrev_b32_e32 v1, 6, v0
	v_and_b32_e32 v2, 63, v0
	v_readfirstlane_b32 s14, v1
	v_lshl_or_b32 v1, s0, 2, v1
	v_lshrrev_b32_e32 v3, 4, v2
	v_and_b32_e32 v4, 15, v2
	v_mul_u32_u24_e32 v5, 25, v1
	v_add_u32_e32 v6, v5, v3
	v_lshlrev_b32_e32 v6, 2, v6
	v_lshlrev_b32_e32 v7, 4, v4
	v_lshlrev_b32_e32 v14, 2, v5
	v_lshrrev_b32_e32 v17, 5, v2
	v_bfe_u32 v18, v2, 4, 1
	v_lshl_or_b32 v19, v17, 3, v7
	v_lshl_or_b32 v19, v18, 2, v19
	v_lshlrev_b32_e32 v46, 1, v19
	v_lshl_or_b32 v46, v1, 9, v46
	s_mul_i32 s14, s14, 7168
	v_lshlrev_b32_e32 v45, 4, v2
	v_add_u32_e32 v45, s14, v45
	v_lshlrev_b32_e32 v47, 2, v2
	v_add_u32_e32 v47, s14, v47
	s_mov_b32 s12, 0x3d23d70a
	s_waitcnt lgkmcnt(0)
	global_load_dword v8, v6, s[10:11]
	global_load_dword v9, v6, s[10:11] offset:16
	global_load_dword v10, v6, s[10:11] offset:32
	global_load_dword v11, v6, s[10:11] offset:48
	global_load_dword v12, v6, s[10:11] offset:64
	global_load_dword v13, v6, s[10:11] offset:80
	global_load_dword v15, v14, s[10:11] offset:96
	s_waitcnt vmcnt(6)
	v_lshl_or_b32 v16, v8, 8, v7
	s_add_u32 s15, s14, 0
	s_mov_b32 m0, s15
	s_nop 0
	global_load_lds_dwordx4 v16, s[8:9]
	s_waitcnt vmcnt(6)
	v_lshl_or_b32 v16, v9, 8, v7
	s_add_u32 s15, s14, 1024
	s_mov_b32 m0, s15
	s_nop 0
	global_load_lds_dwordx4 v16, s[8:9]
	s_waitcnt vmcnt(6)
	v_lshl_or_b32 v16, v10, 8, v7
	s_add_u32 s15, s14, 2048
	s_mov_b32 m0, s15
	s_nop 0
	global_load_lds_dwordx4 v16, s[8:9]
	s_waitcnt vmcnt(6)
	v_lshl_or_b32 v16, v11, 8, v7
	s_add_u32 s15, s14, 3072
	s_mov_b32 m0, s15
	s_nop 0
	global_load_lds_dwordx4 v16, s[8:9]
	s_waitcnt vmcnt(6)
	v_lshl_or_b32 v16, v12, 8, v7
	s_add_u32 s15, s14, 4096
	s_mov_b32 m0, s15
	s_nop 0
	global_load_lds_dwordx4 v16, s[8:9]
	s_waitcnt vmcnt(6)
	v_lshl_or_b32 v16, v13, 8, v7
	s_add_u32 s15, s14, 5120
	s_mov_b32 m0, s15
	s_nop 0
	global_load_lds_dwordx4 v16, s[8:9]
	s_waitcnt vmcnt(6)
	v_lshl_or_b32 v16, v15, 8, v19
	s_add_u32 s15, s14, 6144
	s_mov_b32 m0, s15
	s_nop 0
	global_load_lds_dword v16, s[8:9]
	s_waitcnt vmcnt(0)
	ds_read_b128 v[20:23], v45
	ds_read_b128 v[24:27], v45 offset:1024
	ds_read_b128 v[28:31], v45 offset:2048
	ds_read_b128 v[32:35], v45 offset:3072
	ds_read_b128 v[36:39], v45 offset:4096
	ds_read_b128 v[40:43], v45 offset:5120
	ds_read_b32 v44, v47 offset:6144
	s_waitcnt lgkmcnt(6)
	v_cvt_f32_f16_e32 v48, v20
	v_cvt_f32_f16_sdwa v49, v20 dst_sel:DWORD dst_unused:UNUSED_PAD src0_sel:WORD_1
	v_cvt_f32_f16_e32 v50, v21
	v_cvt_f32_f16_sdwa v51, v21 dst_sel:DWORD dst_unused:UNUSED_PAD src0_sel:WORD_1
	v_cvt_f32_f16_e32 v52, v22
	v_cvt_f32_f16_sdwa v53, v22 dst_sel:DWORD dst_unused:UNUSED_PAD src0_sel:WORD_1
	v_cvt_f32_f16_e32 v54, v23
	v_cvt_f32_f16_sdwa v55, v23 dst_sel:DWORD dst_unused:UNUSED_PAD src0_sel:WORD_1
	s_waitcnt lgkmcnt(5)
	v_cvt_f32_f16_e32 v56, v24
	v_cvt_f32_f16_sdwa v57, v24 dst_sel:DWORD dst_unused:UNUSED_PAD src0_sel:WORD_1
	v_cvt_f32_f16_e32 v58, v25
	v_cvt_f32_f16_sdwa v59, v25 dst_sel:DWORD dst_unused:UNUSED_PAD src0_sel:WORD_1
	v_cvt_f32_f16_e32 v60, v26
	v_cvt_f32_f16_sdwa v61, v26 dst_sel:DWORD dst_unused:UNUSED_PAD src0_sel:WORD_1
	v_cvt_f32_f16_e32 v62, v27
	v_cvt_f32_f16_sdwa v63, v27 dst_sel:DWORD dst_unused:UNUSED_PAD src0_sel:WORD_1
	v_pk_add_f32 v[48:49], v[48:49], v[56:57]
	v_pk_add_f32 v[50:51], v[50:51], v[58:59]
	v_pk_add_f32 v[52:53], v[52:53], v[60:61]
	v_pk_add_f32 v[54:55], v[54:55], v[62:63]
	s_waitcnt lgkmcnt(4)
	v_cvt_f32_f16_e32 v56, v28
	v_cvt_f32_f16_sdwa v57, v28 dst_sel:DWORD dst_unused:UNUSED_PAD src0_sel:WORD_1
	v_cvt_f32_f16_e32 v58, v29
	v_cvt_f32_f16_sdwa v59, v29 dst_sel:DWORD dst_unused:UNUSED_PAD src0_sel:WORD_1
	v_cvt_f32_f16_e32 v60, v30
	v_cvt_f32_f16_sdwa v61, v30 dst_sel:DWORD dst_unused:UNUSED_PAD src0_sel:WORD_1
	v_cvt_f32_f16_e32 v62, v31
	v_cvt_f32_f16_sdwa v63, v31 dst_sel:DWORD dst_unused:UNUSED_PAD src0_sel:WORD_1
	v_pk_add_f32 v[48:49], v[48:49], v[56:57]
	v_pk_add_f32 v[50:51], v[50:51], v[58:59]
	v_pk_add_f32 v[52:53], v[52:53], v[60:61]
	v_pk_add_f32 v[54:55], v[54:55], v[62:63]
	s_waitcnt lgkmcnt(3)
	v_cvt_f32_f16_e32 v56, v32
	v_cvt_f32_f16_sdwa v57, v32 dst_sel:DWORD dst_unused:UNUSED_PAD src0_sel:WORD_1
	v_cvt_f32_f16_e32 v58, v33
	v_cvt_f32_f16_sdwa v59, v33 dst_sel:DWORD dst_unused:UNUSED_PAD src0_sel:WORD_1
	v_cvt_f32_f16_e32 v60, v34
	v_cvt_f32_f16_sdwa v61, v34 dst_sel:DWORD dst_unused:UNUSED_PAD src0_sel:WORD_1
	v_cvt_f32_f16_e32 v62, v35
	v_cvt_f32_f16_sdwa v63, v35 dst_sel:DWORD dst_unused:UNUSED_PAD src0_sel:WORD_1
	v_pk_add_f32 v[48:49], v[48:49], v[56:57]
	v_pk_add_f32 v[50:51], v[50:51], v[58:59]
	v_pk_add_f32 v[52:53], v[52:53], v[60:61]
	v_pk_add_f32 v[54:55], v[54:55], v[62:63]
	s_waitcnt lgkmcnt(2)
	v_cvt_f32_f16_e32 v56, v36
	v_cvt_f32_f16_sdwa v57, v36 dst_sel:DWORD dst_unused:UNUSED_PAD src0_sel:WORD_1
	v_cvt_f32_f16_e32 v58, v37
	v_cvt_f32_f16_sdwa v59, v37 dst_sel:DWORD dst_unused:UNUSED_PAD src0_sel:WORD_1
	v_cvt_f32_f16_e32 v60, v38
	v_cvt_f32_f16_sdwa v61, v38 dst_sel:DWORD dst_unused:UNUSED_PAD src0_sel:WORD_1
	v_cvt_f32_f16_e32 v62, v39
	v_cvt_f32_f16_sdwa v63, v39 dst_sel:DWORD dst_unused:UNUSED_PAD src0_sel:WORD_1
	v_pk_add_f32 v[48:49], v[48:49], v[56:57]
	v_pk_add_f32 v[50:51], v[50:51], v[58:59]
	v_pk_add_f32 v[52:53], v[52:53], v[60:61]
	v_pk_add_f32 v[54:55], v[54:55], v[62:63]
	s_waitcnt lgkmcnt(1)
	v_cvt_f32_f16_e32 v56, v40
	v_cvt_f32_f16_sdwa v57, v40 dst_sel:DWORD dst_unused:UNUSED_PAD src0_sel:WORD_1
	v_cvt_f32_f16_e32 v58, v41
	v_cvt_f32_f16_sdwa v59, v41 dst_sel:DWORD dst_unused:UNUSED_PAD src0_sel:WORD_1
	v_cvt_f32_f16_e32 v60, v42
	v_cvt_f32_f16_sdwa v61, v42 dst_sel:DWORD dst_unused:UNUSED_PAD src0_sel:WORD_1
	v_cvt_f32_f16_e32 v62, v43
	v_cvt_f32_f16_sdwa v63, v43 dst_sel:DWORD dst_unused:UNUSED_PAD src0_sel:WORD_1
	v_pk_add_f32 v[48:49], v[48:49], v[56:57]
	v_pk_add_f32 v[50:51], v[50:51], v[58:59]
	v_pk_add_f32 v[52:53], v[52:53], v[60:61]
	v_pk_add_f32 v[54:55], v[54:55], v[62:63]
	s_waitcnt lgkmcnt(0)
	v_cvt_f32_f16_e32 v56, v44
	v_cvt_f32_f16_sdwa v57, v44 dst_sel:DWORD dst_unused:UNUSED_PAD src0_sel:WORD_1
	v_permlane32_swap_b32_e32 v48, v52
	v_permlane32_swap_b32_e32 v49, v53
	v_permlane32_swap_b32_e32 v50, v54
	v_permlane32_swap_b32_e32 v51, v55
	s_nop 0
	v_pk_add_f32 v[48:49], v[48:49], v[52:53]
	v_pk_add_f32 v[50:51], v[50:51], v[54:55]
	s_nop 1
	v_permlane16_swap_b32_e32 v48, v50
	v_permlane16_swap_b32_e32 v49, v51
	s_nop 0
	v_pk_add_f32 v[48:49], v[48:49], v[50:51]
	s_nop 0
	v_pk_add_f32 v[48:49], v[48:49], v[56:57]
	s_nop 0
	v_pk_mul_f32 v[48:49], v[48:49], s[12:13] op_sel_hi:[1,0]
	global_store_dwordx2 v46, v[48:49], s[4:5] nt
	s_endpgm

	.amdhsa_kernel _Z13gather_kernelPKDv2_DF16_PKiPf
		.amdhsa_group_segment_fixed_size 28672
		.amdhsa_private_segment_fixed_size 0
		.amdhsa_kernarg_size 24
		.amdhsa_user_sgpr_count 2
		.amdhsa_user_sgpr_dispatch_ptr 0
		.amdhsa_user_sgpr_queue_ptr 0
		.amdhsa_user_sgpr_kernarg_segment_ptr 1
		.amdhsa_user_sgpr_dispatch_id 0
		.amdhsa_user_sgpr_kernarg_preload_length 0
		.amdhsa_user_sgpr_kernarg_preload_offset 0
		.amdhsa_user_sgpr_private_segment_size 0
		.amdhsa_uses_dynamic_stack 0
		.amdhsa_enable_private_segment 0
		.amdhsa_system_sgpr_workgroup_id_x 1
		.amdhsa_system_sgpr_workgroup_id_y 0
		.amdhsa_system_sgpr_workgroup_id_z 0
		.amdhsa_system_sgpr_workgroup_info 0
		.amdhsa_system_vgpr_workitem_id 0
		.amdhsa_next_free_vgpr 64
		.amdhsa_next_free_sgpr 16
		.amdhsa_accum_offset 64
		.amdhsa_reserve_vcc 0
		.amdhsa_float_round_mode_32 0
		.amdhsa_float_round_mode_16_64 0
		.amdhsa_float_denorm_mode_32 3
		.amdhsa_float_denorm_mode_16_64 3
		.amdhsa_dx10_clamp 1
		.amdhsa_ieee_mode 1
		.amdhsa_fp16_overflow 0
		.amdhsa_tg_split 0
		.amdhsa_exception_fp_ieee_invalid_op 0
		.amdhsa_exception_fp_denorm_src 0
		.amdhsa_exception_fp_ieee_div_zero 0
		.amdhsa_exception_fp_ieee_overflow 0
		.amdhsa_exception_fp_ieee_underflow 0
		.amdhsa_exception_fp_ieee_inexact 0
		.amdhsa_exception_int_div_zero 0
	.end_amdhsa_kernel

amdhsa.kernels:
  - .agpr_count:     0
    .args:
      - .actual_access:  read_only
        .address_space:  global
        .offset:         0
        .size:           8
        .value_kind:     global_buffer
      - .actual_access:  write_only
        .address_space:  global
        .offset:         8
        .size:           8
        .value_kind:     global_buffer
    .group_segment_fixed_size: 0
    .kernarg_segment_align: 8
    .kernarg_segment_size: 16
    .language:       OpenCL C
    .language_version:
      - 2
      - 0
    .max_flat_workgroup_size: 256
    .name:           _Z10cvt_kernelPKDv4_fPDv4_DF16_
    .private_segment_fixed_size: 0
    .sgpr_count:     24
    .sgpr_spill_count: 0
    .symbol:         _Z10cvt_kernelPKDv4_fPDv4_DF16_.kd
    .uniform_work_group_size: 1
    .uses_dynamic_stack: false
    .vgpr_count:     38
    .vgpr_spill_count: 0
    .wavefront_size: 64
  - .agpr_count:     0
    .args:
      - .actual_access:  read_only
        .address_space:  global
        .offset:         0
        .size:           8
        .value_kind:     global_buffer
      - .actual_access:  read_only
        .address_space:  global
        .offset:         8
        .size:           8
        .value_kind:     global_buffer
      - .actual_access:  write_only
        .address_space:  global
        .offset:         16
        .size:           8
        .value_kind:     global_buffer
    .group_segment_fixed_size: 28672
    .kernarg_segment_align: 8
    .kernarg_segment_size: 24
    .language:       OpenCL C
    .language_version:
      - 2
      - 0
    .max_flat_workgroup_size: 256
    .name:           _Z13gather_kernelPKDv2_DF16_PKiPf
    .private_segment_fixed_size: 0
    .sgpr_count:     22
    .sgpr_spill_count: 0
    .symbol:         _Z13gather_kernelPKDv2_DF16_PKiPf.kd
    .uniform_work_group_size: 1
    .uses_dynamic_stack: false
    .vgpr_count:     64
    .vgpr_spill_count: 0
    .wavefront_size: 64
